# static s_setprio 1 for waves 4-7 over the whole paced attention loop (instead of per-tile alternation)
# baseline (speedup 1.0000x reference)
.Lattn_noprio:
	ds_read_b128 v[160:163], v201 offset:0
	ds_read_b128 v[164:167], v202 offset:0
	ds_read_b128 v[168:171], v203 offset:0
	ds_read_b128 v[172:175], v246 offset:0
	ds_read_b128 v[176:179], v201 offset:4096
	ds_read_b128 v[180:183], v202 offset:4096
	ds_read_b128 v[230:233], v203 offset:4096
	s_waitcnt lgkmcnt(6)
	v_mfma_f32_16x16x32_bf16 v[64:67], v[160:163], v[96:99], 0
	v_mfma_f32_16x16x32_bf16 v[68:71], v[160:163], v[112:115], 0
	ds_read_b128 v[234:237], v246 offset:4096
	s_waitcnt lgkmcnt(6)
	v_mfma_f32_16x16x32_bf16 v[68:71], v[164:167], v[116:119], v[68:71]
	v_mfma_f32_16x16x32_bf16 v[64:67], v[164:167], v[100:103], v[64:67]
	ds_read_b128 v[160:163], v201 offset:8192
	s_waitcnt lgkmcnt(6)
	v_mfma_f32_16x16x32_bf16 v[64:67], v[168:171], v[104:107], v[64:67]
	v_mfma_f32_16x16x32_bf16 v[68:71], v[168:171], v[120:123], v[68:71]
	ds_read_b128 v[164:167], v202 offset:8192
	s_waitcnt lgkmcnt(6)
	v_mfma_f32_16x16x32_bf16 v[68:71], v[172:175], v[124:127], v[68:71]
	v_mfma_f32_16x16x32_bf16 v[64:67], v[172:175], v[108:111], v[64:67]
	ds_read_b128 v[168:171], v203 offset:8192
	s_waitcnt lgkmcnt(6)
	v_mfma_f32_16x16x32_bf16 v[72:75], v[176:179], v[96:99], 0
	s_nop 7
	s_nop 1
	v_exp_f32_e32 v64, v64
	v_mfma_f32_16x16x32_bf16 v[76:79], v[176:179], v[112:115], 0
	v_exp_f32_e32 v68, v68
	ds_read_b128 v[172:175], v246 offset:8192
	s_waitcnt lgkmcnt(6)
	v_mfma_f32_16x16x32_bf16 v[76:79], v[180:183], v[116:119], v[76:79]
	v_exp_f32_e32 v65, v65
	v_exp_f32_e32 v69, v69
	v_mfma_f32_16x16x32_bf16 v[72:75], v[180:183], v[100:103], v[72:75]
	v_exp_f32_e32 v66, v66
	ds_read_b128 v[176:179], v201 offset:12288
	s_waitcnt lgkmcnt(6)
	v_mfma_f32_16x16x32_bf16 v[72:75], v[230:233], v[104:107], v[72:75]
	v_exp_f32_e32 v70, v70
	v_exp_f32_e32 v67, v67
	v_mfma_f32_16x16x32_bf16 v[76:79], v[230:233], v[120:123], v[76:79]
	v_exp_f32_e32 v71, v71
	v_add_f32_e32 v220, v64, v65
	ds_read_b128 v[180:183], v202 offset:12288
	s_waitcnt lgkmcnt(6)
	v_mfma_f32_16x16x32_bf16 v[76:79], v[234:237], v[124:127], v[76:79]
	v_add_f32_e32 v221, v68, v69
	v_add_f32_e32 v220, v220, v66
	v_add_f32_e32 v221, v221, v70
	v_mfma_f32_16x16x32_bf16 v[72:75], v[234:237], v[108:111], v[72:75]
	v_add_f32_e32 v220, v220, v67
	v_add_f32_e32 v221, v221, v71
	ds_read_b128 v[230:233], v203 offset:12288
	s_waitcnt lgkmcnt(6)
	v_mfma_f32_16x16x32_bf16 v[80:83], v[160:163], v[96:99], 0
	s_nop 7
	s_nop 1
	v_exp_f32_e32 v72, v72
	v_exp_f32_e32 v76, v76
	v_mfma_f32_16x16x32_bf16 v[84:87], v[160:163], v[112:115], 0
	v_exp_f32_e32 v73, v73
	v_exp_f32_e32 v77, v77
	ds_read_b128 v[234:237], v246 offset:12288
	s_waitcnt lgkmcnt(6)
	v_mfma_f32_16x16x32_bf16 v[84:87], v[164:167], v[116:119], v[84:87]
	v_exp_f32_e32 v74, v74
	v_exp_f32_e32 v78, v78
	v_mfma_f32_16x16x32_bf16 v[80:83], v[164:167], v[100:103], v[80:83]
	v_exp_f32_e32 v75, v75
	v_exp_f32_e32 v79, v79
	s_waitcnt lgkmcnt(5)
	v_mfma_f32_16x16x32_bf16 v[80:83], v[168:171], v[104:107], v[80:83]
	v_add_f32_e32 v220, v220, v72
	v_add_f32_e32 v221, v221, v76
	v_add_f32_e32 v220, v220, v73
	v_add_f32_e32 v221, v221, v77
	v_mfma_f32_16x16x32_bf16 v[84:87], v[168:171], v[120:123], v[84:87]
	v_add_f32_e32 v220, v220, v74
	v_add_f32_e32 v221, v221, v78
	v_add_f32_e32 v220, v220, v75
	v_add_f32_e32 v221, v221, v79
	s_waitcnt lgkmcnt(4)
	v_mfma_f32_16x16x32_bf16 v[84:87], v[172:175], v[124:127], v[84:87]
	v_cvt_pk_bf16_f32 v216, v64, v65
	v_cvt_pk_bf16_f32 v217, v66, v67
	v_cvt_pk_bf16_f32 v238, v68, v69
	v_cvt_pk_bf16_f32 v239, v70, v71
	v_mfma_f32_16x16x32_bf16 v[80:83], v[172:175], v[108:111], v[80:83]
	v_cvt_pk_bf16_f32 v218, v72, v73
	v_cvt_pk_bf16_f32 v219, v74, v75
	v_cvt_pk_bf16_f32 v240, v76, v77
	v_cvt_pk_bf16_f32 v241, v78, v79
	s_waitcnt lgkmcnt(3)
	v_mfma_f32_16x16x32_bf16 v[88:91], v[176:179], v[96:99], 0
	s_nop 7
	s_nop 1
	v_exp_f32_e32 v80, v80
	v_exp_f32_e32 v84, v84
	v_mfma_f32_16x16x32_bf16 v[92:95], v[176:179], v[112:115], 0
	v_exp_f32_e32 v81, v81
	s_waitcnt lgkmcnt(2)
	v_mfma_f32_16x16x32_bf16 v[92:95], v[180:183], v[116:119], v[92:95]
	v_exp_f32_e32 v85, v85
	v_exp_f32_e32 v82, v82
	v_mfma_f32_16x16x32_bf16 v[88:91], v[180:183], v[100:103], v[88:91]
	v_exp_f32_e32 v86, v86
	s_waitcnt lgkmcnt(1)
	v_mfma_f32_16x16x32_bf16 v[88:91], v[230:233], v[104:107], v[88:91]
	v_exp_f32_e32 v83, v83
	v_exp_f32_e32 v87, v87
	v_mfma_f32_16x16x32_bf16 v[92:95], v[230:233], v[120:123], v[92:95]
	v_add_f32_e32 v220, v220, v80
	v_add_f32_e32 v221, v221, v84
	v_add_f32_e32 v220, v220, v81
	s_waitcnt lgkmcnt(0)
	v_mfma_f32_16x16x32_bf16 v[92:95], v[234:237], v[124:127], v[92:95]
	v_add_f32_e32 v221, v221, v85
	v_add_f32_e32 v220, v220, v82
	v_add_f32_e32 v221, v221, v86
	v_mfma_f32_16x16x32_bf16 v[88:91], v[234:237], v[108:111], v[88:91]
	v_add_f32_e32 v220, v220, v83
	v_add_f32_e32 v221, v221, v87
	s_waitcnt lgkmcnt(0)
	s_barrier
	ds_read_b128 v[160:163], v201 offset:16384
	ds_read_b128 v[164:167], v209 offset:0
	ds_read_b128 v[168:171], v202 offset:16384
	ds_read_b128 v[172:175], v209 offset:2048
	ds_read_b128 v[176:179], v203 offset:16384
	ds_read_b128 v[180:183], v209 offset:4096
	ds_read_b128 v[230:233], v246 offset:16384
.LBB0_734:
	s_waitcnt lgkmcnt(6)
	v_mfma_f32_16x16x32_bf16 v[64:67], v[160:163], v[96:99], 0
	v_exp_f32_e32 v88, v88
	v_mfma_f32_16x16x32_bf16 v[68:71], v[160:163], v[112:115], 0
	v_exp_f32_e32 v92, v92
	ds_read_b128 v[234:237], v209 offset:6144
	s_add_u32 s16, s22, s10
	s_addc_u32 s17, s23, s11
	s_add_u32 s15, s22, s12
	s_addc_u32 s14, s23, s13
	s_add_u32 s8, s16, 0x3bc00200
	s_addc_u32 s9, s17, 0
	s_add_u32 s6, s15, 0x23a50000
	s_addc_u32 s7, s14, 0
	s_waitcnt lgkmcnt(6)
	v_mfma_f32_16x16x32_bf16 v[0:3], v[164:167], v[216:219], v[0:3]
	v_cvt_pk_bf16_f32 v242, v80, v81
	v_mfma_f32_16x16x32_bf16 v[4:7], v[164:167], v[238:241], v[4:7]
	v_exp_f32_e32 v89, v89
	ds_read_b128 v[160:163], v201 offset:20480
	s_waitcnt vmcnt(4)
	ds_write_b128 v225, v[152:155] offset:49152
	s_waitcnt lgkmcnt(7)
	v_mfma_f32_16x16x32_bf16 v[68:71], v[168:171], v[116:119], v[68:71]
	v_exp_f32_e32 v93, v93
	v_mfma_f32_16x16x32_bf16 v[64:67], v[168:171], v[100:103], v[64:67]
	v_cvt_pk_bf16_f32 v243, v82, v83
	ds_read_b128 v[164:167], v209 offset:8192
	ds_write_b128 v226, v[156:159] offset:49152
	s_waitcnt lgkmcnt(8)
	v_mfma_f32_16x16x32_bf16 v[12:15], v[172:175], v[238:241], v[12:15]
	v_exp_f32_e32 v90, v90
	v_mfma_f32_16x16x32_bf16 v[8:11], v[172:175], v[216:219], v[8:11]
	v_exp_f32_e32 v94, v94
	ds_read_b128 v[168:171], v202 offset:20480
	ds_write_b64 v227, v[132:133] offset:32768
	s_waitcnt lgkmcnt(9)
	v_mfma_f32_16x16x32_bf16 v[64:67], v[176:179], v[104:107], v[64:67]
	v_cvt_pk_bf16_f32 v204, v84, v85
	v_mfma_f32_16x16x32_bf16 v[68:71], v[176:179], v[120:123], v[68:71]
	v_exp_f32_e32 v91, v91
	ds_read_b128 v[172:175], v209 offset:10240
	ds_write_b64 v228, v[134:135] offset:32768
	s_waitcnt lgkmcnt(10)
	v_mfma_f32_16x16x32_bf16 v[16:19], v[180:183], v[216:219], v[16:19]
	v_exp_f32_e32 v95, v95
	v_mfma_f32_16x16x32_bf16 v[20:23], v[180:183], v[238:241], v[20:23]
	v_cvt_pk_bf16_f32 v205, v86, v87
	v_add_f32_e32 v220, v220, v88
	ds_read_b128 v[176:179], v203 offset:20480
	ds_write_b64 v229, v[128:129] offset:32768
	s_waitcnt lgkmcnt(11)
	v_mfma_f32_16x16x32_bf16 v[68:71], v[230:233], v[124:127], v[68:71]
	v_add_f32_e32 v221, v221, v92
	v_add_f32_e32 v220, v220, v89
	v_mfma_f32_16x16x32_bf16 v[64:67], v[230:233], v[108:111], v[64:67]
	v_add_f32_e32 v221, v221, v93
	v_cvt_pk_bf16_f32 v244, v88, v89
	ds_read_b128 v[180:183], v209 offset:12288
	ds_write_b64 v184, v[130:131] offset:32768
	s_waitcnt lgkmcnt(12)
	v_mfma_f32_16x16x32_bf16 v[28:31], v[234:237], v[238:241], v[28:31]
	v_cvt_pk_bf16_f32 v245, v90, v91
	v_cvt_pk_bf16_f32 v206, v92, v93
	v_mfma_f32_16x16x32_bf16 v[24:27], v[234:237], v[216:219], v[24:27]
	v_cvt_pk_bf16_f32 v207, v94, v95
	ds_read_b128 v[230:233], v246 offset:20480
	global_load_dwordx4 v[132:135], v198, s[8:9]
	s_waitcnt lgkmcnt(12)
	v_mfma_f32_16x16x32_bf16 v[72:75], v[160:163], v[96:99], 0
	v_add_f32_e32 v220, v220, v90
	v_add_f32_e32 v221, v221, v94
	v_mfma_f32_16x16x32_bf16 v[76:79], v[160:163], v[112:115], 0
	v_add_f32_e32 v220, v220, v91
	v_add_f32_e32 v221, v221, v95
	ds_read_b128 v[234:237], v209 offset:14336
	global_load_dwordx4 v[128:131], v199, s[8:9]
	s_waitcnt lgkmcnt(11)
	v_mfma_f32_16x16x32_bf16 v[32:35], v[164:167], v[216:219], v[32:35]
	v_add_f32_e32 v194, v194, v220
	v_add_f32_e32 v195, v195, v221
	v_mfma_f32_16x16x32_bf16 v[36:39], v[164:167], v[238:241], v[36:39]
	v_exp_f32_e32 v64, v64
	ds_read_b128 v[160:163], v201 offset:24576
	global_load_dwordx4 v[152:155], v196, s[6:7]
	s_waitcnt lgkmcnt(10)
	v_mfma_f32_16x16x32_bf16 v[76:79], v[168:171], v[116:119], v[76:79]
	v_exp_f32_e32 v68, v68
	v_mfma_f32_16x16x32_bf16 v[72:75], v[168:171], v[100:103], v[72:75]
	v_exp_f32_e32 v65, v65
	ds_read_b128 v[164:167], v210 offset:0
	global_load_dwordx4 v[156:159], v197, s[6:7]
	s_waitcnt lgkmcnt(9)
	v_mfma_f32_16x16x32_bf16 v[44:47], v[172:175], v[238:241], v[44:47]
	v_exp_f32_e32 v69, v69
	v_mfma_f32_16x16x32_bf16 v[40:43], v[172:175], v[216:219], v[40:43]
	v_exp_f32_e32 v66, v66
	ds_read_b128 v[168:171], v202 offset:24576
	s_waitcnt lgkmcnt(8)
	v_mfma_f32_16x16x32_bf16 v[72:75], v[176:179], v[104:107], v[72:75]
	v_exp_f32_e32 v70, v70
	v_mfma_f32_16x16x32_bf16 v[76:79], v[176:179], v[120:123], v[76:79]
	v_exp_f32_e32 v67, v67
	ds_read_b128 v[172:175], v210 offset:2048
	s_waitcnt lgkmcnt(7)
	v_mfma_f32_16x16x32_bf16 v[48:51], v[180:183], v[216:219], v[48:51]
	v_exp_f32_e32 v71, v71
	v_mfma_f32_16x16x32_bf16 v[52:55], v[180:183], v[238:241], v[52:55]
	v_add_f32_e32 v220, v64, v65
	ds_read_b128 v[176:179], v203 offset:24576
	s_waitcnt lgkmcnt(6)
	v_mfma_f32_16x16x32_bf16 v[76:79], v[230:233], v[124:127], v[76:79]
	v_add_f32_e32 v221, v68, v69
	v_mfma_f32_16x16x32_bf16 v[72:75], v[230:233], v[108:111], v[72:75]
	v_add_f32_e32 v220, v220, v66
	ds_read_b128 v[180:183], v210 offset:4096
	s_waitcnt lgkmcnt(6)
	v_mfma_f32_16x16x32_bf16 v[60:63], v[234:237], v[238:241], v[60:63]
	v_add_f32_e32 v221, v221, v70
	v_add_f32_e32 v220, v220, v67
	v_mfma_f32_16x16x32_bf16 v[56:59], v[234:237], v[216:219], v[56:59]
	v_add_f32_e32 v221, v221, v71
	ds_read_b128 v[230:233], v246 offset:24576
	s_waitcnt lgkmcnt(6)
	v_mfma_f32_16x16x32_bf16 v[80:83], v[160:163], v[96:99], 0
	v_exp_f32_e32 v72, v72
	v_mfma_f32_16x16x32_bf16 v[84:87], v[160:163], v[112:115], 0
	v_exp_f32_e32 v76, v76
	ds_read_b128 v[234:237], v210 offset:6144
	s_waitcnt lgkmcnt(6)
	v_mfma_f32_16x16x32_bf16 v[0:3], v[164:167], v[242:245], v[0:3]
	v_exp_f32_e32 v73, v73
	v_mfma_f32_16x16x32_bf16 v[4:7], v[164:167], v[204:207], v[4:7]
	v_exp_f32_e32 v77, v77
	ds_read_b128 v[160:163], v201 offset:28672
	s_waitcnt lgkmcnt(6)
	v_mfma_f32_16x16x32_bf16 v[84:87], v[168:171], v[116:119], v[84:87]
	v_exp_f32_e32 v74, v74
	v_mfma_f32_16x16x32_bf16 v[80:83], v[168:171], v[100:103], v[80:83]
	v_exp_f32_e32 v78, v78
	ds_read_b128 v[164:167], v210 offset:8192
	s_waitcnt lgkmcnt(6)
	v_mfma_f32_16x16x32_bf16 v[12:15], v[172:175], v[204:207], v[12:15]
	v_exp_f32_e32 v75, v75
	v_mfma_f32_16x16x32_bf16 v[8:11], v[172:175], v[242:245], v[8:11]
	v_exp_f32_e32 v79, v79
	ds_read_b128 v[168:171], v202 offset:28672
	s_waitcnt lgkmcnt(6)
	v_mfma_f32_16x16x32_bf16 v[80:83], v[176:179], v[104:107], v[80:83]
	v_add_f32_e32 v220, v220, v72
	v_add_f32_e32 v221, v221, v76
	v_mfma_f32_16x16x32_bf16 v[84:87], v[176:179], v[120:123], v[84:87]
	v_add_f32_e32 v220, v220, v73
	ds_read_b128 v[172:175], v210 offset:10240
	s_waitcnt lgkmcnt(6)
	v_mfma_f32_16x16x32_bf16 v[16:19], v[180:183], v[242:245], v[16:19]
	v_add_f32_e32 v221, v221, v77
	v_add_f32_e32 v220, v220, v74
	v_mfma_f32_16x16x32_bf16 v[20:23], v[180:183], v[204:207], v[20:23]
	v_add_f32_e32 v221, v221, v78
	ds_read_b128 v[176:179], v203 offset:28672
	s_waitcnt lgkmcnt(6)
	v_mfma_f32_16x16x32_bf16 v[84:87], v[230:233], v[124:127], v[84:87]
	v_add_f32_e32 v220, v220, v75
	v_add_f32_e32 v221, v221, v79
	v_mfma_f32_16x16x32_bf16 v[80:83], v[230:233], v[108:111], v[80:83]
	v_cvt_pk_bf16_f32 v216, v64, v65
	ds_read_b128 v[180:183], v210 offset:12288
	s_waitcnt lgkmcnt(6)
	v_mfma_f32_16x16x32_bf16 v[28:31], v[234:237], v[204:207], v[28:31]
	v_cvt_pk_bf16_f32 v217, v66, v67
	v_cvt_pk_bf16_f32 v238, v68, v69
	v_mfma_f32_16x16x32_bf16 v[24:27], v[234:237], v[242:245], v[24:27]
	v_cvt_pk_bf16_f32 v239, v70, v71
	ds_read_b128 v[230:233], v246 offset:28672
	s_waitcnt lgkmcnt(6)
	v_mfma_f32_16x16x32_bf16 v[88:91], v[160:163], v[96:99], 0
	v_exp_f32_e32 v80, v80
	v_mfma_f32_16x16x32_bf16 v[92:95], v[160:163], v[112:115], 0
	v_exp_f32_e32 v84, v84
	ds_read_b128 v[234:237], v210 offset:14336
	s_waitcnt lgkmcnt(6)
	v_mfma_f32_16x16x32_bf16 v[32:35], v[164:167], v[242:245], v[32:35]
	v_exp_f32_e32 v81, v81
	v_mfma_f32_16x16x32_bf16 v[36:39], v[164:167], v[204:207], v[36:39]
	v_exp_f32_e32 v85, v85
	ds_read_b128 v[160:163], v201 offset:32768
	s_waitcnt lgkmcnt(6)
	v_mfma_f32_16x16x32_bf16 v[92:95], v[168:171], v[116:119], v[92:95]
	v_exp_f32_e32 v82, v82
	v_mfma_f32_16x16x32_bf16 v[88:91], v[168:171], v[100:103], v[88:91]
	v_exp_f32_e32 v86, v86
	ds_read_b128 v[164:167], v209 offset:16384
	s_waitcnt lgkmcnt(6)
	v_mfma_f32_16x16x32_bf16 v[44:47], v[172:175], v[204:207], v[44:47]
	v_exp_f32_e32 v83, v83
	v_mfma_f32_16x16x32_bf16 v[40:43], v[172:175], v[242:245], v[40:43]
	v_exp_f32_e32 v87, v87
	ds_read_b128 v[168:171], v202 offset:32768
	s_waitcnt lgkmcnt(6)
	v_mfma_f32_16x16x32_bf16 v[88:91], v[176:179], v[104:107], v[88:91]
	v_add_f32_e32 v220, v220, v80
	v_add_f32_e32 v221, v221, v84
	v_mfma_f32_16x16x32_bf16 v[92:95], v[176:179], v[120:123], v[92:95]
	v_add_f32_e32 v220, v220, v81
	ds_read_b128 v[172:175], v209 offset:18432
	s_waitcnt lgkmcnt(6)
	v_mfma_f32_16x16x32_bf16 v[48:51], v[180:183], v[242:245], v[48:51]
	v_add_f32_e32 v221, v221, v85
	v_add_f32_e32 v220, v220, v82
	v_mfma_f32_16x16x32_bf16 v[52:55], v[180:183], v[204:207], v[52:55]
	v_add_f32_e32 v221, v221, v86
	ds_read_b128 v[176:179], v203 offset:32768
	s_waitcnt lgkmcnt(6)
	v_mfma_f32_16x16x32_bf16 v[92:95], v[230:233], v[124:127], v[92:95]
	v_add_f32_e32 v220, v220, v83
	v_add_f32_e32 v221, v221, v87
	v_mfma_f32_16x16x32_bf16 v[88:91], v[230:233], v[108:111], v[88:91]
	v_cvt_pk_bf16_f32 v218, v72, v73
	ds_read_b128 v[180:183], v209 offset:20480
	s_waitcnt lgkmcnt(6)
	v_mfma_f32_16x16x32_bf16 v[60:63], v[234:237], v[204:207], v[60:63]
	v_cvt_pk_bf16_f32 v219, v74, v75
	v_cvt_pk_bf16_f32 v240, v76, v77
	v_mfma_f32_16x16x32_bf16 v[56:59], v[234:237], v[242:245], v[56:59]
	v_cvt_pk_bf16_f32 v241, v78, v79
	ds_read_b128 v[230:233], v246 offset:32768
	s_waitcnt lgkmcnt(6)
	v_mfma_f32_16x16x32_bf16 v[64:67], v[160:163], v[96:99], 0
	v_exp_f32_e32 v88, v88
	v_mfma_f32_16x16x32_bf16 v[68:71], v[160:163], v[112:115], 0
	v_exp_f32_e32 v92, v92
	ds_read_b128 v[234:237], v209 offset:22528
	s_add_u32 s8, s16, 0x3bc00280
	s_addc_u32 s9, s17, 0
	s_add_u32 s6, s15, 0x23a60000
	s_addc_u32 s7, s14, 0
	s_waitcnt lgkmcnt(6)
	v_mfma_f32_16x16x32_bf16 v[0:3], v[164:167], v[216:219], v[0:3]
	v_cvt_pk_bf16_f32 v242, v80, v81
	v_mfma_f32_16x16x32_bf16 v[4:7], v[164:167], v[238:241], v[4:7]
	v_exp_f32_e32 v89, v89
	ds_read_b128 v[160:163], v201 offset:36864
	s_waitcnt vmcnt(4)
	ds_write_b128 v225, v[136:139] offset:0
	s_waitcnt lgkmcnt(7)
	v_mfma_f32_16x16x32_bf16 v[68:71], v[168:171], v[116:119], v[68:71]
	v_exp_f32_e32 v93, v93
	v_mfma_f32_16x16x32_bf16 v[64:67], v[168:171], v[100:103], v[64:67]
	v_cvt_pk_bf16_f32 v243, v82, v83
	ds_read_b128 v[164:167], v209 offset:24576
	ds_write_b128 v226, v[140:143] offset:0
	s_waitcnt lgkmcnt(8)
	v_mfma_f32_16x16x32_bf16 v[12:15], v[172:175], v[238:241], v[12:15]
	v_exp_f32_e32 v90, v90
	v_mfma_f32_16x16x32_bf16 v[8:11], v[172:175], v[216:219], v[8:11]
	v_exp_f32_e32 v94, v94
	ds_read_b128 v[168:171], v202 offset:36864
	ds_write_b64 v227, v[148:149] offset:49152
	s_waitcnt lgkmcnt(9)
	v_mfma_f32_16x16x32_bf16 v[64:67], v[176:179], v[104:107], v[64:67]
	v_cvt_pk_bf16_f32 v204, v84, v85
	v_mfma_f32_16x16x32_bf16 v[68:71], v[176:179], v[120:123], v[68:71]
	v_exp_f32_e32 v91, v91
	ds_read_b128 v[172:175], v209 offset:26624
	ds_write_b64 v228, v[150:151] offset:49152
	s_waitcnt lgkmcnt(10)
	v_mfma_f32_16x16x32_bf16 v[16:19], v[180:183], v[216:219], v[16:19]
	v_exp_f32_e32 v95, v95
	v_mfma_f32_16x16x32_bf16 v[20:23], v[180:183], v[238:241], v[20:23]
	v_cvt_pk_bf16_f32 v205, v86, v87
	v_add_f32_e32 v220, v220, v88
	ds_read_b128 v[176:179], v203 offset:36864
	ds_write_b64 v229, v[144:145] offset:49152
	s_waitcnt lgkmcnt(11)
	v_mfma_f32_16x16x32_bf16 v[68:71], v[230:233], v[124:127], v[68:71]
	v_add_f32_e32 v221, v221, v92
	v_add_f32_e32 v220, v220, v89
	v_mfma_f32_16x16x32_bf16 v[64:67], v[230:233], v[108:111], v[64:67]
	v_add_f32_e32 v221, v221, v93
	v_cvt_pk_bf16_f32 v244, v88, v89
	ds_read_b128 v[180:183], v209 offset:28672
	ds_write_b64 v184, v[146:147] offset:49152
	s_waitcnt lgkmcnt(12)
	v_mfma_f32_16x16x32_bf16 v[28:31], v[234:237], v[238:241], v[28:31]
	v_cvt_pk_bf16_f32 v245, v90, v91
	v_cvt_pk_bf16_f32 v206, v92, v93
	v_mfma_f32_16x16x32_bf16 v[24:27], v[234:237], v[216:219], v[24:27]
	v_cvt_pk_bf16_f32 v207, v94, v95
	ds_read_b128 v[230:233], v246 offset:36864
	global_load_dwordx4 v[148:151], v198, s[8:9]
	s_waitcnt lgkmcnt(12)
	v_mfma_f32_16x16x32_bf16 v[72:75], v[160:163], v[96:99], 0
	v_add_f32_e32 v220, v220, v90
	v_add_f32_e32 v221, v221, v94
	v_mfma_f32_16x16x32_bf16 v[76:79], v[160:163], v[112:115], 0
	v_add_f32_e32 v220, v220, v91
	v_add_f32_e32 v221, v221, v95
	ds_read_b128 v[234:237], v209 offset:30720
	global_load_dwordx4 v[144:147], v199, s[8:9]
	s_waitcnt lgkmcnt(11)
	v_mfma_f32_16x16x32_bf16 v[32:35], v[164:167], v[216:219], v[32:35]
	v_add_f32_e32 v194, v194, v220
	v_add_f32_e32 v195, v195, v221
	v_mfma_f32_16x16x32_bf16 v[36:39], v[164:167], v[238:241], v[36:39]
	v_exp_f32_e32 v64, v64
	ds_read_b128 v[160:163], v201 offset:40960
	global_load_dwordx4 v[136:139], v196, s[6:7]
	s_waitcnt lgkmcnt(10)
	v_mfma_f32_16x16x32_bf16 v[76:79], v[168:171], v[116:119], v[76:79]
	v_exp_f32_e32 v68, v68
	v_mfma_f32_16x16x32_bf16 v[72:75], v[168:171], v[100:103], v[72:75]
	v_exp_f32_e32 v65, v65
	ds_read_b128 v[164:167], v210 offset:16384
	global_load_dwordx4 v[140:143], v197, s[6:7]
	s_waitcnt lgkmcnt(9)
	v_mfma_f32_16x16x32_bf16 v[44:47], v[172:175], v[238:241], v[44:47]
	v_exp_f32_e32 v69, v69
	v_mfma_f32_16x16x32_bf16 v[40:43], v[172:175], v[216:219], v[40:43]
	v_exp_f32_e32 v66, v66
	ds_read_b128 v[168:171], v202 offset:40960
	s_waitcnt lgkmcnt(8)
	v_mfma_f32_16x16x32_bf16 v[72:75], v[176:179], v[104:107], v[72:75]
	v_exp_f32_e32 v70, v70
	v_mfma_f32_16x16x32_bf16 v[76:79], v[176:179], v[120:123], v[76:79]
	v_exp_f32_e32 v67, v67
	ds_read_b128 v[172:175], v210 offset:18432
	s_waitcnt lgkmcnt(7)
	v_mfma_f32_16x16x32_bf16 v[48:51], v[180:183], v[216:219], v[48:51]
	v_exp_f32_e32 v71, v71
	v_mfma_f32_16x16x32_bf16 v[52:55], v[180:183], v[238:241], v[52:55]
	v_add_f32_e32 v220, v64, v65
	ds_read_b128 v[176:179], v203 offset:40960
	s_waitcnt lgkmcnt(6)
	v_mfma_f32_16x16x32_bf16 v[76:79], v[230:233], v[124:127], v[76:79]
	v_add_f32_e32 v221, v68, v69
	v_mfma_f32_16x16x32_bf16 v[72:75], v[230:233], v[108:111], v[72:75]
	v_add_f32_e32 v220, v220, v66
	ds_read_b128 v[180:183], v210 offset:20480
	s_waitcnt lgkmcnt(6)
	v_mfma_f32_16x16x32_bf16 v[60:63], v[234:237], v[238:241], v[60:63]
	v_add_f32_e32 v221, v221, v70
	v_add_f32_e32 v220, v220, v67
	v_mfma_f32_16x16x32_bf16 v[56:59], v[234:237], v[216:219], v[56:59]
	v_add_f32_e32 v221, v221, v71
	ds_read_b128 v[230:233], v246 offset:40960
	s_waitcnt lgkmcnt(6)
	v_mfma_f32_16x16x32_bf16 v[80:83], v[160:163], v[96:99], 0
	v_exp_f32_e32 v72, v72
	v_mfma_f32_16x16x32_bf16 v[84:87], v[160:163], v[112:115], 0
	v_exp_f32_e32 v76, v76
	ds_read_b128 v[234:237], v210 offset:22528
	s_waitcnt lgkmcnt(6)
	v_mfma_f32_16x16x32_bf16 v[0:3], v[164:167], v[242:245], v[0:3]
	v_exp_f32_e32 v73, v73
	v_mfma_f32_16x16x32_bf16 v[4:7], v[164:167], v[204:207], v[4:7]
	v_exp_f32_e32 v77, v77
	ds_read_b128 v[160:163], v201 offset:45056
	s_waitcnt lgkmcnt(6)
	v_mfma_f32_16x16x32_bf16 v[84:87], v[168:171], v[116:119], v[84:87]
	v_exp_f32_e32 v74, v74
	v_mfma_f32_16x16x32_bf16 v[80:83], v[168:171], v[100:103], v[80:83]
	v_exp_f32_e32 v78, v78
	ds_read_b128 v[164:167], v210 offset:24576
	s_waitcnt lgkmcnt(6)
	v_mfma_f32_16x16x32_bf16 v[12:15], v[172:175], v[204:207], v[12:15]
	v_exp_f32_e32 v75, v75
	v_mfma_f32_16x16x32_bf16 v[8:11], v[172:175], v[242:245], v[8:11]
	v_exp_f32_e32 v79, v79
	ds_read_b128 v[168:171], v202 offset:45056
	s_waitcnt lgkmcnt(6)
	v_mfma_f32_16x16x32_bf16 v[80:83], v[176:179], v[104:107], v[80:83]
	v_add_f32_e32 v220, v220, v72
	v_add_f32_e32 v221, v221, v76
	v_mfma_f32_16x16x32_bf16 v[84:87], v[176:179], v[120:123], v[84:87]
	v_add_f32_e32 v220, v220, v73
	ds_read_b128 v[172:175], v210 offset:26624
	s_waitcnt lgkmcnt(6)
	v_mfma_f32_16x16x32_bf16 v[16:19], v[180:183], v[242:245], v[16:19]
	v_add_f32_e32 v221, v221, v77
	v_add_f32_e32 v220, v220, v74
	v_mfma_f32_16x16x32_bf16 v[20:23], v[180:183], v[204:207], v[20:23]
	v_add_f32_e32 v221, v221, v78
	ds_read_b128 v[176:179], v203 offset:45056
	s_waitcnt lgkmcnt(6)
	v_mfma_f32_16x16x32_bf16 v[84:87], v[230:233], v[124:127], v[84:87]
	v_add_f32_e32 v220, v220, v75
	v_add_f32_e32 v221, v221, v79
	v_mfma_f32_16x16x32_bf16 v[80:83], v[230:233], v[108:111], v[80:83]
	v_cvt_pk_bf16_f32 v216, v64, v65
	ds_read_b128 v[180:183], v210 offset:28672
	s_waitcnt lgkmcnt(6)
	v_mfma_f32_16x16x32_bf16 v[28:31], v[234:237], v[204:207], v[28:31]
	v_cvt_pk_bf16_f32 v217, v66, v67
	v_cvt_pk_bf16_f32 v238, v68, v69
	v_mfma_f32_16x16x32_bf16 v[24:27], v[234:237], v[242:245], v[24:27]
	v_cvt_pk_bf16_f32 v239, v70, v71
	ds_read_b128 v[230:233], v246 offset:45056
	s_waitcnt lgkmcnt(6)
	v_mfma_f32_16x16x32_bf16 v[88:91], v[160:163], v[96:99], 0
	v_exp_f32_e32 v80, v80
	v_mfma_f32_16x16x32_bf16 v[92:95], v[160:163], v[112:115], 0
	v_exp_f32_e32 v84, v84
	ds_read_b128 v[234:237], v210 offset:30720
	s_waitcnt lgkmcnt(6)
	v_mfma_f32_16x16x32_bf16 v[32:35], v[164:167], v[242:245], v[32:35]
	v_exp_f32_e32 v81, v81
	v_mfma_f32_16x16x32_bf16 v[36:39], v[164:167], v[204:207], v[36:39]
	v_exp_f32_e32 v85, v85
	s_waitcnt lgkmcnt(5)
	v_mfma_f32_16x16x32_bf16 v[92:95], v[168:171], v[116:119], v[92:95]
	v_exp_f32_e32 v82, v82
	v_mfma_f32_16x16x32_bf16 v[88:91], v[168:171], v[100:103], v[88:91]
	v_exp_f32_e32 v86, v86
	s_waitcnt lgkmcnt(4)
	v_mfma_f32_16x16x32_bf16 v[44:47], v[172:175], v[204:207], v[44:47]
	v_exp_f32_e32 v83, v83
	v_mfma_f32_16x16x32_bf16 v[40:43], v[172:175], v[242:245], v[40:43]
	v_exp_f32_e32 v87, v87
	s_waitcnt lgkmcnt(3)
	v_mfma_f32_16x16x32_bf16 v[88:91], v[176:179], v[104:107], v[88:91]
	v_add_f32_e32 v220, v220, v80
	v_add_f32_e32 v221, v221, v84
	v_mfma_f32_16x16x32_bf16 v[92:95], v[176:179], v[120:123], v[92:95]
	v_add_f32_e32 v220, v220, v81
	s_waitcnt lgkmcnt(0)
	s_barrier
	ds_read_b128 v[160:163], v201 offset:49152
	ds_read_b128 v[164:167], v209 offset:32768
	ds_read_b128 v[168:171], v202 offset:49152
	ds_read_b128 v[172:175], v209 offset:34816
	v_mfma_f32_16x16x32_bf16 v[48:51], v[180:183], v[242:245], v[48:51]
	v_add_f32_e32 v221, v221, v85
	v_add_f32_e32 v220, v220, v82
	v_mfma_f32_16x16x32_bf16 v[52:55], v[180:183], v[204:207], v[52:55]
	v_add_f32_e32 v221, v221, v86
	ds_read_b128 v[176:179], v203 offset:49152
	v_mfma_f32_16x16x32_bf16 v[92:95], v[230:233], v[124:127], v[92:95]
	v_add_f32_e32 v220, v220, v83
	v_add_f32_e32 v221, v221, v87
	v_mfma_f32_16x16x32_bf16 v[88:91], v[230:233], v[108:111], v[88:91]
	v_cvt_pk_bf16_f32 v218, v72, v73
	ds_read_b128 v[180:183], v209 offset:36864
	v_mfma_f32_16x16x32_bf16 v[60:63], v[234:237], v[204:207], v[60:63]
	v_cvt_pk_bf16_f32 v219, v74, v75
	v_cvt_pk_bf16_f32 v240, v76, v77
	v_mfma_f32_16x16x32_bf16 v[56:59], v[234:237], v[242:245], v[56:59]
	v_cvt_pk_bf16_f32 v241, v78, v79
	ds_read_b128 v[230:233], v246 offset:49152
	s_waitcnt lgkmcnt(6)
	v_mfma_f32_16x16x32_bf16 v[64:67], v[160:163], v[96:99], 0
	v_exp_f32_e32 v88, v88
	v_mfma_f32_16x16x32_bf16 v[68:71], v[160:163], v[112:115], 0
	v_exp_f32_e32 v92, v92
	ds_read_b128 v[234:237], v209 offset:38912
	s_add_u32 s8, s16, 0x3bc00300
	s_addc_u32 s9, s17, 0
	s_add_u32 s6, s15, 0x23a70000
	s_addc_u32 s7, s14, 0
	s_waitcnt lgkmcnt(6)
	v_mfma_f32_16x16x32_bf16 v[0:3], v[164:167], v[216:219], v[0:3]
	v_cvt_pk_bf16_f32 v242, v80, v81
	v_mfma_f32_16x16x32_bf16 v[4:7], v[164:167], v[238:241], v[4:7]
	v_exp_f32_e32 v89, v89
	ds_read_b128 v[160:163], v201 offset:53248
	s_waitcnt vmcnt(4)
	ds_write_b128 v225, v[152:155] offset:16384
	s_waitcnt lgkmcnt(7)
	v_mfma_f32_16x16x32_bf16 v[68:71], v[168:171], v[116:119], v[68:71]
	v_exp_f32_e32 v93, v93
	v_mfma_f32_16x16x32_bf16 v[64:67], v[168:171], v[100:103], v[64:67]
	v_cvt_pk_bf16_f32 v243, v82, v83
	ds_read_b128 v[164:167], v209 offset:40960
	ds_write_b128 v226, v[156:159] offset:16384
	s_waitcnt lgkmcnt(8)
	v_mfma_f32_16x16x32_bf16 v[12:15], v[172:175], v[238:241], v[12:15]
	v_exp_f32_e32 v90, v90
	v_mfma_f32_16x16x32_bf16 v[8:11], v[172:175], v[216:219], v[8:11]
	v_exp_f32_e32 v94, v94
	ds_read_b128 v[168:171], v202 offset:53248
	ds_write_b64 v227, v[132:133] offset:0
	s_waitcnt lgkmcnt(9)
	v_mfma_f32_16x16x32_bf16 v[64:67], v[176:179], v[104:107], v[64:67]
	v_cvt_pk_bf16_f32 v204, v84, v85
	v_mfma_f32_16x16x32_bf16 v[68:71], v[176:179], v[120:123], v[68:71]
	v_exp_f32_e32 v91, v91
	ds_read_b128 v[172:175], v209 offset:43008
	ds_write_b64 v228, v[134:135] offset:0
	s_waitcnt lgkmcnt(10)
	v_mfma_f32_16x16x32_bf16 v[16:19], v[180:183], v[216:219], v[16:19]
	v_exp_f32_e32 v95, v95
	v_mfma_f32_16x16x32_bf16 v[20:23], v[180:183], v[238:241], v[20:23]
	v_cvt_pk_bf16_f32 v205, v86, v87
	v_add_f32_e32 v220, v220, v88
	ds_read_b128 v[176:179], v203 offset:53248
	ds_write_b64 v229, v[128:129] offset:0
	s_waitcnt lgkmcnt(11)
	v_mfma_f32_16x16x32_bf16 v[68:71], v[230:233], v[124:127], v[68:71]
	v_add_f32_e32 v221, v221, v92
	v_add_f32_e32 v220, v220, v89
	v_mfma_f32_16x16x32_bf16 v[64:67], v[230:233], v[108:111], v[64:67]
	v_add_f32_e32 v221, v221, v93
	v_cvt_pk_bf16_f32 v244, v88, v89
	ds_read_b128 v[180:183], v209 offset:45056
	ds_write_b64 v184, v[130:131] offset:0
	s_waitcnt lgkmcnt(12)
	v_mfma_f32_16x16x32_bf16 v[28:31], v[234:237], v[238:241], v[28:31]
	v_cvt_pk_bf16_f32 v245, v90, v91
	v_cvt_pk_bf16_f32 v206, v92, v93
	v_mfma_f32_16x16x32_bf16 v[24:27], v[234:237], v[216:219], v[24:27]
	v_cvt_pk_bf16_f32 v207, v94, v95
	ds_read_b128 v[230:233], v246 offset:53248
	global_load_dwordx4 v[132:135], v198, s[8:9]
	s_waitcnt lgkmcnt(12)
	v_mfma_f32_16x16x32_bf16 v[72:75], v[160:163], v[96:99], 0
	v_add_f32_e32 v220, v220, v90
	v_add_f32_e32 v221, v221, v94
	v_mfma_f32_16x16x32_bf16 v[76:79], v[160:163], v[112:115], 0
	v_add_f32_e32 v220, v220, v91
	v_add_f32_e32 v221, v221, v95
	ds_read_b128 v[234:237], v209 offset:47104
	global_load_dwordx4 v[128:131], v199, s[8:9]
	s_waitcnt lgkmcnt(11)
	v_mfma_f32_16x16x32_bf16 v[32:35], v[164:167], v[216:219], v[32:35]
	v_add_f32_e32 v194, v194, v220
	v_add_f32_e32 v195, v195, v221
	v_mfma_f32_16x16x32_bf16 v[36:39], v[164:167], v[238:241], v[36:39]
	v_exp_f32_e32 v64, v64
	ds_read_b128 v[160:163], v201 offset:57344
	global_load_dwordx4 v[152:155], v196, s[6:7]
	s_waitcnt lgkmcnt(10)
	v_mfma_f32_16x16x32_bf16 v[76:79], v[168:171], v[116:119], v[76:79]
	v_exp_f32_e32 v68, v68
	v_mfma_f32_16x16x32_bf16 v[72:75], v[168:171], v[100:103], v[72:75]
	v_exp_f32_e32 v65, v65
	ds_read_b128 v[164:167], v210 offset:32768
	global_load_dwordx4 v[156:159], v197, s[6:7]
	s_waitcnt lgkmcnt(9)
	v_mfma_f32_16x16x32_bf16 v[44:47], v[172:175], v[238:241], v[44:47]
	v_exp_f32_e32 v69, v69
	v_mfma_f32_16x16x32_bf16 v[40:43], v[172:175], v[216:219], v[40:43]
	v_exp_f32_e32 v66, v66
	ds_read_b128 v[168:171], v202 offset:57344
	s_waitcnt lgkmcnt(8)
	v_mfma_f32_16x16x32_bf16 v[72:75], v[176:179], v[104:107], v[72:75]
	v_exp_f32_e32 v70, v70
	v_mfma_f32_16x16x32_bf16 v[76:79], v[176:179], v[120:123], v[76:79]
	v_exp_f32_e32 v67, v67
	ds_read_b128 v[172:175], v210 offset:34816
	s_waitcnt lgkmcnt(7)
	v_mfma_f32_16x16x32_bf16 v[48:51], v[180:183], v[216:219], v[48:51]
	v_exp_f32_e32 v71, v71
	v_mfma_f32_16x16x32_bf16 v[52:55], v[180:183], v[238:241], v[52:55]
	v_add_f32_e32 v220, v64, v65
	ds_read_b128 v[176:179], v203 offset:57344
	s_waitcnt lgkmcnt(6)
	v_mfma_f32_16x16x32_bf16 v[76:79], v[230:233], v[124:127], v[76:79]
	v_add_f32_e32 v221, v68, v69
	v_mfma_f32_16x16x32_bf16 v[72:75], v[230:233], v[108:111], v[72:75]
	v_add_f32_e32 v220, v220, v66
	ds_read_b128 v[180:183], v210 offset:36864
	s_waitcnt lgkmcnt(6)
	v_mfma_f32_16x16x32_bf16 v[60:63], v[234:237], v[238:241], v[60:63]
	v_add_f32_e32 v221, v221, v70
	v_add_f32_e32 v220, v220, v67
	v_mfma_f32_16x16x32_bf16 v[56:59], v[234:237], v[216:219], v[56:59]
	v_add_f32_e32 v221, v221, v71
	ds_read_b128 v[230:233], v246 offset:57344
	s_waitcnt lgkmcnt(6)
	v_mfma_f32_16x16x32_bf16 v[80:83], v[160:163], v[96:99], 0
	v_exp_f32_e32 v72, v72
	v_mfma_f32_16x16x32_bf16 v[84:87], v[160:163], v[112:115], 0
	v_exp_f32_e32 v76, v76
	ds_read_b128 v[234:237], v210 offset:38912
	s_waitcnt lgkmcnt(6)
	v_mfma_f32_16x16x32_bf16 v[0:3], v[164:167], v[242:245], v[0:3]
	v_exp_f32_e32 v73, v73
	v_mfma_f32_16x16x32_bf16 v[4:7], v[164:167], v[204:207], v[4:7]
	v_exp_f32_e32 v77, v77
	ds_read_b128 v[160:163], v201 offset:61440
	s_waitcnt lgkmcnt(6)
	v_mfma_f32_16x16x32_bf16 v[84:87], v[168:171], v[116:119], v[84:87]
	v_exp_f32_e32 v74, v74
	v_mfma_f32_16x16x32_bf16 v[80:83], v[168:171], v[100:103], v[80:83]
	v_exp_f32_e32 v78, v78
	ds_read_b128 v[164:167], v210 offset:40960
	s_waitcnt lgkmcnt(6)
	v_mfma_f32_16x16x32_bf16 v[12:15], v[172:175], v[204:207], v[12:15]
	v_exp_f32_e32 v75, v75
	v_mfma_f32_16x16x32_bf16 v[8:11], v[172:175], v[242:245], v[8:11]
	v_exp_f32_e32 v79, v79
	ds_read_b128 v[168:171], v202 offset:61440
	s_waitcnt lgkmcnt(6)
	v_mfma_f32_16x16x32_bf16 v[80:83], v[176:179], v[104:107], v[80:83]
	v_add_f32_e32 v220, v220, v72
	v_add_f32_e32 v221, v221, v76
	v_mfma_f32_16x16x32_bf16 v[84:87], v[176:179], v[120:123], v[84:87]
	v_add_f32_e32 v220, v220, v73
	ds_read_b128 v[172:175], v210 offset:43008
	s_waitcnt lgkmcnt(6)
	v_mfma_f32_16x16x32_bf16 v[16:19], v[180:183], v[242:245], v[16:19]
	v_add_f32_e32 v221, v221, v77
	v_add_f32_e32 v220, v220, v74
	v_mfma_f32_16x16x32_bf16 v[20:23], v[180:183], v[204:207], v[20:23]
	v_add_f32_e32 v221, v221, v78
	ds_read_b128 v[176:179], v203 offset:61440
	s_waitcnt lgkmcnt(6)
	v_mfma_f32_16x16x32_bf16 v[84:87], v[230:233], v[124:127], v[84:87]
	v_add_f32_e32 v220, v220, v75
	v_add_f32_e32 v221, v221, v79
	v_mfma_f32_16x16x32_bf16 v[80:83], v[230:233], v[108:111], v[80:83]
	v_cvt_pk_bf16_f32 v216, v64, v65
	ds_read_b128 v[180:183], v210 offset:45056
	s_waitcnt lgkmcnt(6)
	v_mfma_f32_16x16x32_bf16 v[28:31], v[234:237], v[204:207], v[28:31]
	v_cvt_pk_bf16_f32 v217, v66, v67
	v_cvt_pk_bf16_f32 v238, v68, v69
	v_mfma_f32_16x16x32_bf16 v[24:27], v[234:237], v[242:245], v[24:27]
	v_cvt_pk_bf16_f32 v239, v70, v71
	ds_read_b128 v[230:233], v246 offset:61440
	s_waitcnt lgkmcnt(6)
	v_mfma_f32_16x16x32_bf16 v[88:91], v[160:163], v[96:99], 0
	v_exp_f32_e32 v80, v80
	v_mfma_f32_16x16x32_bf16 v[92:95], v[160:163], v[112:115], 0
	v_exp_f32_e32 v84, v84
	ds_read_b128 v[234:237], v210 offset:47104
	s_waitcnt lgkmcnt(6)
	v_mfma_f32_16x16x32_bf16 v[32:35], v[164:167], v[242:245], v[32:35]
	v_exp_f32_e32 v81, v81
	v_mfma_f32_16x16x32_bf16 v[36:39], v[164:167], v[204:207], v[36:39]
	v_exp_f32_e32 v85, v85
	ds_read_b128 v[160:163], v201 offset:0
	s_waitcnt lgkmcnt(6)
	v_mfma_f32_16x16x32_bf16 v[92:95], v[168:171], v[116:119], v[92:95]
	v_exp_f32_e32 v82, v82
	v_mfma_f32_16x16x32_bf16 v[88:91], v[168:171], v[100:103], v[88:91]
	v_exp_f32_e32 v86, v86
	ds_read_b128 v[164:167], v209 offset:49152
	s_waitcnt lgkmcnt(6)
	v_mfma_f32_16x16x32_bf16 v[44:47], v[172:175], v[204:207], v[44:47]
	v_exp_f32_e32 v83, v83
	v_mfma_f32_16x16x32_bf16 v[40:43], v[172:175], v[242:245], v[40:43]
	v_exp_f32_e32 v87, v87
	ds_read_b128 v[168:171], v202 offset:0
	s_waitcnt lgkmcnt(6)
	v_mfma_f32_16x16x32_bf16 v[88:91], v[176:179], v[104:107], v[88:91]
	v_add_f32_e32 v220, v220, v80
	v_add_f32_e32 v221, v221, v84
	v_mfma_f32_16x16x32_bf16 v[92:95], v[176:179], v[120:123], v[92:95]
	v_add_f32_e32 v220, v220, v81
	ds_read_b128 v[172:175], v209 offset:51200
	s_waitcnt lgkmcnt(6)
	v_mfma_f32_16x16x32_bf16 v[48:51], v[180:183], v[242:245], v[48:51]
	v_add_f32_e32 v221, v221, v85
	v_add_f32_e32 v220, v220, v82
	v_mfma_f32_16x16x32_bf16 v[52:55], v[180:183], v[204:207], v[52:55]
	v_add_f32_e32 v221, v221, v86
	ds_read_b128 v[176:179], v203 offset:0
	s_waitcnt lgkmcnt(6)
	v_mfma_f32_16x16x32_bf16 v[92:95], v[230:233], v[124:127], v[92:95]
	v_add_f32_e32 v220, v220, v83
	v_add_f32_e32 v221, v221, v87
	v_mfma_f32_16x16x32_bf16 v[88:91], v[230:233], v[108:111], v[88:91]
	v_cvt_pk_bf16_f32 v218, v72, v73
	ds_read_b128 v[180:183], v209 offset:53248
	s_waitcnt lgkmcnt(6)
	v_mfma_f32_16x16x32_bf16 v[60:63], v[234:237], v[204:207], v[60:63]
	v_cvt_pk_bf16_f32 v219, v74, v75
	v_cvt_pk_bf16_f32 v240, v76, v77
	v_mfma_f32_16x16x32_bf16 v[56:59], v[234:237], v[242:245], v[56:59]
	v_cvt_pk_bf16_f32 v241, v78, v79
	ds_read_b128 v[230:233], v246 offset:0
	s_waitcnt lgkmcnt(6)
	v_mfma_f32_16x16x32_bf16 v[64:67], v[160:163], v[96:99], 0
	v_exp_f32_e32 v88, v88
	v_mfma_f32_16x16x32_bf16 v[68:71], v[160:163], v[112:115], 0
	v_exp_f32_e32 v92, v92
	ds_read_b128 v[234:237], v209 offset:55296
	s_add_u32 s8, s16, 0x3bc00380
	s_addc_u32 s9, s17, 0
	s_add_u32 s6, s15, 0x23a80000
	s_addc_u32 s7, s14, 0
	s_waitcnt lgkmcnt(6)
	v_mfma_f32_16x16x32_bf16 v[0:3], v[164:167], v[216:219], v[0:3]
	v_cvt_pk_bf16_f32 v242, v80, v81
	v_mfma_f32_16x16x32_bf16 v[4:7], v[164:167], v[238:241], v[4:7]
	v_exp_f32_e32 v89, v89
	ds_read_b128 v[160:163], v201 offset:4096
	s_waitcnt vmcnt(4)
	ds_write_b128 v225, v[136:139] offset:32768
	s_waitcnt lgkmcnt(7)
	v_mfma_f32_16x16x32_bf16 v[68:71], v[168:171], v[116:119], v[68:71]
	v_exp_f32_e32 v93, v93
	v_mfma_f32_16x16x32_bf16 v[64:67], v[168:171], v[100:103], v[64:67]
	v_cvt_pk_bf16_f32 v243, v82, v83
	ds_read_b128 v[164:167], v209 offset:57344
	ds_write_b128 v226, v[140:143] offset:32768
	s_waitcnt lgkmcnt(8)
	v_mfma_f32_16x16x32_bf16 v[12:15], v[172:175], v[238:241], v[12:15]
	v_exp_f32_e32 v90, v90
	v_mfma_f32_16x16x32_bf16 v[8:11], v[172:175], v[216:219], v[8:11]
	v_exp_f32_e32 v94, v94
	ds_read_b128 v[168:171], v202 offset:4096
	ds_write_b64 v227, v[148:149] offset:16384
	s_waitcnt lgkmcnt(9)
	v_mfma_f32_16x16x32_bf16 v[64:67], v[176:179], v[104:107], v[64:67]
	v_cvt_pk_bf16_f32 v204, v84, v85
	v_mfma_f32_16x16x32_bf16 v[68:71], v[176:179], v[120:123], v[68:71]
	v_exp_f32_e32 v91, v91
	ds_read_b128 v[172:175], v209 offset:59392
	ds_write_b64 v228, v[150:151] offset:16384
	s_waitcnt lgkmcnt(10)
	v_mfma_f32_16x16x32_bf16 v[16:19], v[180:183], v[216:219], v[16:19]
	v_exp_f32_e32 v95, v95
	v_mfma_f32_16x16x32_bf16 v[20:23], v[180:183], v[238:241], v[20:23]
	v_cvt_pk_bf16_f32 v205, v86, v87
	v_add_f32_e32 v220, v220, v88
	ds_read_b128 v[176:179], v203 offset:4096
	ds_write_b64 v229, v[144:145] offset:16384
	s_waitcnt lgkmcnt(11)
	v_mfma_f32_16x16x32_bf16 v[68:71], v[230:233], v[124:127], v[68:71]
	v_add_f32_e32 v221, v221, v92
	v_add_f32_e32 v220, v220, v89
	v_mfma_f32_16x16x32_bf16 v[64:67], v[230:233], v[108:111], v[64:67]
	v_add_f32_e32 v221, v221, v93
	v_cvt_pk_bf16_f32 v244, v88, v89
	ds_read_b128 v[180:183], v209 offset:61440
	ds_write_b64 v184, v[146:147] offset:16384
	s_waitcnt lgkmcnt(12)
	v_mfma_f32_16x16x32_bf16 v[28:31], v[234:237], v[238:241], v[28:31]
	v_cvt_pk_bf16_f32 v245, v90, v91
	v_cvt_pk_bf16_f32 v206, v92, v93
	v_mfma_f32_16x16x32_bf16 v[24:27], v[234:237], v[216:219], v[24:27]
	v_cvt_pk_bf16_f32 v207, v94, v95
	ds_read_b128 v[230:233], v246 offset:4096
	global_load_dwordx4 v[148:151], v198, s[8:9]
	s_waitcnt lgkmcnt(12)
	v_mfma_f32_16x16x32_bf16 v[72:75], v[160:163], v[96:99], 0
	v_add_f32_e32 v220, v220, v90
	v_add_f32_e32 v221, v221, v94
	v_mfma_f32_16x16x32_bf16 v[76:79], v[160:163], v[112:115], 0
	v_add_f32_e32 v220, v220, v91
	v_add_f32_e32 v221, v221, v95
	ds_read_b128 v[234:237], v209 offset:63488
	global_load_dwordx4 v[144:147], v199, s[8:9]
	s_waitcnt lgkmcnt(11)
	v_mfma_f32_16x16x32_bf16 v[32:35], v[164:167], v[216:219], v[32:35]
	v_add_f32_e32 v194, v194, v220
	v_add_f32_e32 v195, v195, v221
	v_mfma_f32_16x16x32_bf16 v[36:39], v[164:167], v[238:241], v[36:39]
	v_exp_f32_e32 v64, v64
	ds_read_b128 v[160:163], v201 offset:8192
	global_load_dwordx4 v[136:139], v196, s[6:7]
	s_waitcnt lgkmcnt(10)
	v_mfma_f32_16x16x32_bf16 v[76:79], v[168:171], v[116:119], v[76:79]
	v_exp_f32_e32 v68, v68
	v_mfma_f32_16x16x32_bf16 v[72:75], v[168:171], v[100:103], v[72:75]
	v_exp_f32_e32 v65, v65
	ds_read_b128 v[164:167], v210 offset:49152
	global_load_dwordx4 v[140:143], v197, s[6:7]
	s_waitcnt lgkmcnt(9)
	v_mfma_f32_16x16x32_bf16 v[44:47], v[172:175], v[238:241], v[44:47]
	v_exp_f32_e32 v69, v69
	v_mfma_f32_16x16x32_bf16 v[40:43], v[172:175], v[216:219], v[40:43]
	v_exp_f32_e32 v66, v66
	ds_read_b128 v[168:171], v202 offset:8192
	s_waitcnt lgkmcnt(8)
	v_mfma_f32_16x16x32_bf16 v[72:75], v[176:179], v[104:107], v[72:75]
	v_exp_f32_e32 v70, v70
	v_mfma_f32_16x16x32_bf16 v[76:79], v[176:179], v[120:123], v[76:79]
	v_exp_f32_e32 v67, v67
	ds_read_b128 v[172:175], v210 offset:51200
	s_waitcnt lgkmcnt(7)
	v_mfma_f32_16x16x32_bf16 v[48:51], v[180:183], v[216:219], v[48:51]
	v_exp_f32_e32 v71, v71
	v_mfma_f32_16x16x32_bf16 v[52:55], v[180:183], v[238:241], v[52:55]
	v_add_f32_e32 v220, v64, v65
	ds_read_b128 v[176:179], v203 offset:8192
	s_waitcnt lgkmcnt(6)
	v_mfma_f32_16x16x32_bf16 v[76:79], v[230:233], v[124:127], v[76:79]
	v_add_f32_e32 v221, v68, v69
	v_mfma_f32_16x16x32_bf16 v[72:75], v[230:233], v[108:111], v[72:75]
	v_add_f32_e32 v220, v220, v66
	ds_read_b128 v[180:183], v210 offset:53248
	s_waitcnt lgkmcnt(6)
	v_mfma_f32_16x16x32_bf16 v[60:63], v[234:237], v[238:241], v[60:63]
	v_add_f32_e32 v221, v221, v70
	v_add_f32_e32 v220, v220, v67
	v_mfma_f32_16x16x32_bf16 v[56:59], v[234:237], v[216:219], v[56:59]
	v_add_f32_e32 v221, v221, v71
	ds_read_b128 v[230:233], v246 offset:8192
	s_waitcnt lgkmcnt(6)
	v_mfma_f32_16x16x32_bf16 v[80:83], v[160:163], v[96:99], 0
	v_exp_f32_e32 v72, v72
	v_mfma_f32_16x16x32_bf16 v[84:87], v[160:163], v[112:115], 0
	v_exp_f32_e32 v76, v76
	ds_read_b128 v[234:237], v210 offset:55296
	s_waitcnt lgkmcnt(6)
	v_mfma_f32_16x16x32_bf16 v[0:3], v[164:167], v[242:245], v[0:3]
	v_exp_f32_e32 v73, v73
	v_mfma_f32_16x16x32_bf16 v[4:7], v[164:167], v[204:207], v[4:7]
	v_exp_f32_e32 v77, v77
	ds_read_b128 v[160:163], v201 offset:12288
	s_waitcnt lgkmcnt(6)
	v_mfma_f32_16x16x32_bf16 v[84:87], v[168:171], v[116:119], v[84:87]
	v_exp_f32_e32 v74, v74
	v_mfma_f32_16x16x32_bf16 v[80:83], v[168:171], v[100:103], v[80:83]
	v_exp_f32_e32 v78, v78
	ds_read_b128 v[164:167], v210 offset:57344
	s_waitcnt lgkmcnt(6)
	v_mfma_f32_16x16x32_bf16 v[12:15], v[172:175], v[204:207], v[12:15]
	v_exp_f32_e32 v75, v75
	v_mfma_f32_16x16x32_bf16 v[8:11], v[172:175], v[242:245], v[8:11]
	v_exp_f32_e32 v79, v79
	ds_read_b128 v[168:171], v202 offset:12288
	s_waitcnt lgkmcnt(6)
	v_mfma_f32_16x16x32_bf16 v[80:83], v[176:179], v[104:107], v[80:83]
	v_add_f32_e32 v220, v220, v72
	v_add_f32_e32 v221, v221, v76
	v_mfma_f32_16x16x32_bf16 v[84:87], v[176:179], v[120:123], v[84:87]
	v_add_f32_e32 v220, v220, v73
	ds_read_b128 v[172:175], v210 offset:59392
	s_add_u32 s10, s10, 0x200
	s_addc_u32 s11, s11, 0
	s_add_u32 s12, s12, 0x40000
	s_addc_u32 s13, s13, 0
	s_add_i32 s4, s4, 4
	s_cmpk_lt_u32 s4, 0x104
	s_cselect_b64 s[6:7], -1, 0
	s_and_b64 s[6:7], s[0:1], s[6:7]
	s_and_b64 vcc, exec, s[6:7]
	s_waitcnt lgkmcnt(6)
	v_mfma_f32_16x16x32_bf16 v[16:19], v[180:183], v[242:245], v[16:19]
	v_add_f32_e32 v221, v221, v77
	v_add_f32_e32 v220, v220, v74
	v_mfma_f32_16x16x32_bf16 v[20:23], v[180:183], v[204:207], v[20:23]
	v_add_f32_e32 v221, v221, v78
	ds_read_b128 v[176:179], v203 offset:12288
	s_waitcnt lgkmcnt(6)
	v_mfma_f32_16x16x32_bf16 v[84:87], v[230:233], v[124:127], v[84:87]
	v_add_f32_e32 v220, v220, v75
	v_add_f32_e32 v221, v221, v79
	v_mfma_f32_16x16x32_bf16 v[80:83], v[230:233], v[108:111], v[80:83]
	v_cvt_pk_bf16_f32 v216, v64, v65
	ds_read_b128 v[180:183], v210 offset:61440
	s_waitcnt lgkmcnt(6)
	v_mfma_f32_16x16x32_bf16 v[28:31], v[234:237], v[204:207], v[28:31]
	v_cvt_pk_bf16_f32 v217, v66, v67
	v_cvt_pk_bf16_f32 v238, v68, v69
	v_mfma_f32_16x16x32_bf16 v[24:27], v[234:237], v[242:245], v[24:27]
	v_cvt_pk_bf16_f32 v239, v70, v71
	ds_read_b128 v[230:233], v246 offset:12288
	s_waitcnt lgkmcnt(6)
	v_mfma_f32_16x16x32_bf16 v[88:91], v[160:163], v[96:99], 0
	v_exp_f32_e32 v80, v80
	v_mfma_f32_16x16x32_bf16 v[92:95], v[160:163], v[112:115], 0
	v_exp_f32_e32 v84, v84
	ds_read_b128 v[234:237], v210 offset:63488
	s_waitcnt lgkmcnt(6)
	v_mfma_f32_16x16x32_bf16 v[32:35], v[164:167], v[242:245], v[32:35]
	v_exp_f32_e32 v81, v81
	v_mfma_f32_16x16x32_bf16 v[36:39], v[164:167], v[204:207], v[36:39]
	v_exp_f32_e32 v85, v85
	s_waitcnt lgkmcnt(5)
	v_mfma_f32_16x16x32_bf16 v[92:95], v[168:171], v[116:119], v[92:95]
	v_exp_f32_e32 v82, v82
	v_mfma_f32_16x16x32_bf16 v[88:91], v[168:171], v[100:103], v[88:91]
	v_exp_f32_e32 v86, v86
	s_waitcnt lgkmcnt(4)
	v_mfma_f32_16x16x32_bf16 v[44:47], v[172:175], v[204:207], v[44:47]
	v_exp_f32_e32 v83, v83
	v_mfma_f32_16x16x32_bf16 v[40:43], v[172:175], v[242:245], v[40:43]
	v_exp_f32_e32 v87, v87
	s_waitcnt lgkmcnt(3)
	v_mfma_f32_16x16x32_bf16 v[88:91], v[176:179], v[104:107], v[88:91]
	v_add_f32_e32 v220, v220, v80
	v_add_f32_e32 v221, v221, v84
	v_mfma_f32_16x16x32_bf16 v[92:95], v[176:179], v[120:123], v[92:95]
	v_add_f32_e32 v220, v220, v81
	s_waitcnt lgkmcnt(0)
	s_barrier
	ds_read_b128 v[160:163], v201 offset:16384
	ds_read_b128 v[164:167], v209 offset:0
	ds_read_b128 v[168:171], v202 offset:16384
	ds_read_b128 v[172:175], v209 offset:2048
	v_mfma_f32_16x16x32_bf16 v[48:51], v[180:183], v[242:245], v[48:51]
	v_add_f32_e32 v221, v221, v85
	v_add_f32_e32 v220, v220, v82
	v_mfma_f32_16x16x32_bf16 v[52:55], v[180:183], v[204:207], v[52:55]
	v_add_f32_e32 v221, v221, v86
	ds_read_b128 v[176:179], v203 offset:16384
	v_mfma_f32_16x16x32_bf16 v[92:95], v[230:233], v[124:127], v[92:95]
	v_add_f32_e32 v220, v220, v83
	v_add_f32_e32 v221, v221, v87
	v_mfma_f32_16x16x32_bf16 v[88:91], v[230:233], v[108:111], v[88:91]
	v_cvt_pk_bf16_f32 v218, v72, v73
	ds_read_b128 v[180:183], v209 offset:4096
	v_mfma_f32_16x16x32_bf16 v[60:63], v[234:237], v[204:207], v[60:63]
	v_cvt_pk_bf16_f32 v219, v74, v75
	v_cvt_pk_bf16_f32 v240, v76, v77
	v_mfma_f32_16x16x32_bf16 v[56:59], v[234:237], v[242:245], v[56:59]
	v_cvt_pk_bf16_f32 v241, v78, v79
	ds_read_b128 v[230:233], v246 offset:16384
	s_cbranch_vccnz .LBB0_734
	s_setprio 0
	s_waitcnt vmcnt(0)
	s_nop 7
	s_nop 7
	ds_swizzle_b32 v64, v194 offset:swizzle(SWAP,16)
	s_waitcnt lgkmcnt(0)
	v_add_f32_e32 v194, v194, v64
	v_mov_b32_e32 v65, v194
	s_nop 1
	v_permlane32_swap_b32_e32 v194, v65
	v_add_f32_e32 v194, v194, v65
	s_nop 0
	v_rcp_f32_e32 v66, v194
	ds_swizzle_b32 v64, v195 offset:swizzle(SWAP,16)
	s_waitcnt lgkmcnt(0)
	v_add_f32_e32 v195, v195, v64
	v_mov_b32_e32 v65, v195
	s_nop 1
	v_permlane32_swap_b32_e32 v195, v65
	v_add_f32_e32 v195, v195, v65
	s_nop 0
	v_rcp_f32_e32 v67, v195
	v_readlane_b32 s100, v250, 8
	v_mbcnt_lo_u32_b32 v68, -1, 0
	v_mbcnt_hi_u32_b32 v68, -1, v68
	v_and_b32_e32 v69, 15, v68
	v_lshrrev_b32_e32 v70, 4, v68
	s_lshr_b32 s101, s100, 1
	v_add_u32_e32 v69, s101, v69
	v_lshlrev_b32_e32 v69, 12, v69
	v_and_b32_e32 v71, 1, v70
	v_lshlrev_b32_e32 v71, 5, v71
	v_and_b32_e32 v70, 2, v70
	v_lshl_add_u32 v71, v70, 3, v71
	v_add_u32_e32 v70, v69, v71
	v_add_u32_e32 v71, 0x10000, v70
	v_mul_f32_e32 v0, v0, v66
	v_mul_f32_e32 v1, v1, v66
	v_mul_f32_e32 v2, v2, v66
	v_mul_f32_e32 v3, v3, v66
	v_mul_f32_e32 v8, v8, v66
	v_mul_f32_e32 v9, v9, v66
	v_mul_f32_e32 v10, v10, v66
	v_mul_f32_e32 v11, v11, v66
	v_cvt_pk_bf16_f32 v72, v0, v1
	v_cvt_pk_bf16_f32 v73, v2, v3
	v_cvt_pk_bf16_f32 v74, v8, v9
	v_cvt_pk_bf16_f32 v75, v10, v11
	s_nop 1
	v_permlane16_swap_b32_e32 v72, v74
	v_permlane16_swap_b32_e32 v73, v75
	s_nop 1
	global_store_dwordx4 v70, v[72:75], s[58:59] offset:0
	v_mul_f32_e32 v16, v16, v66
	v_mul_f32_e32 v17, v17, v66
	v_mul_f32_e32 v18, v18, v66
	v_mul_f32_e32 v19, v19, v66
	v_mul_f32_e32 v24, v24, v66
	v_mul_f32_e32 v25, v25, v66
	v_mul_f32_e32 v26, v26, v66
	v_mul_f32_e32 v27, v27, v66
	v_cvt_pk_bf16_f32 v76, v16, v17
	v_cvt_pk_bf16_f32 v77, v18, v19
	v_cvt_pk_bf16_f32 v78, v24, v25
	v_cvt_pk_bf16_f32 v79, v26, v27
	s_nop 1
	v_permlane16_swap_b32_e32 v76, v78
	v_permlane16_swap_b32_e32 v77, v79
	s_nop 1
	global_store_dwordx4 v70, v[76:79], s[58:59] offset:64
	v_mul_f32_e32 v32, v32, v66
	v_mul_f32_e32 v33, v33, v66
	v_mul_f32_e32 v34, v34, v66
	v_mul_f32_e32 v35, v35, v66
	v_mul_f32_e32 v40, v40, v66
	v_mul_f32_e32 v41, v41, v66
	v_mul_f32_e32 v42, v42, v66
	v_mul_f32_e32 v43, v43, v66
	v_cvt_pk_bf16_f32 v80, v32, v33
	v_cvt_pk_bf16_f32 v81, v34, v35
	v_cvt_pk_bf16_f32 v82, v40, v41
	v_cvt_pk_bf16_f32 v83, v42, v43
	s_nop 1
	v_permlane16_swap_b32_e32 v80, v82
	v_permlane16_swap_b32_e32 v81, v83
	s_nop 1
	global_store_dwordx4 v70, v[80:83], s[58:59] offset:128
	v_mul_f32_e32 v48, v48, v66
	v_mul_f32_e32 v49, v49, v66
	v_mul_f32_e32 v50, v50, v66
	v_mul_f32_e32 v51, v51, v66
	v_mul_f32_e32 v56, v56, v66
	v_mul_f32_e32 v57, v57, v66
	v_mul_f32_e32 v58, v58, v66
	v_mul_f32_e32 v59, v59, v66
	v_cvt_pk_bf16_f32 v84, v48, v49
	v_cvt_pk_bf16_f32 v85, v50, v51
	v_cvt_pk_bf16_f32 v86, v56, v57
	v_cvt_pk_bf16_f32 v87, v58, v59
	s_nop 1
	v_permlane16_swap_b32_e32 v84, v86
	v_permlane16_swap_b32_e32 v85, v87
	s_nop 1
	global_store_dwordx4 v70, v[84:87], s[58:59] offset:192
	v_mul_f32_e32 v4, v4, v67
	v_mul_f32_e32 v5, v5, v67
	v_mul_f32_e32 v6, v6, v67
	v_mul_f32_e32 v7, v7, v67
	v_mul_f32_e32 v12, v12, v67
	v_mul_f32_e32 v13, v13, v67
	v_mul_f32_e32 v14, v14, v67
	v_mul_f32_e32 v15, v15, v67
	v_cvt_pk_bf16_f32 v88, v4, v5
	v_cvt_pk_bf16_f32 v89, v6, v7
	v_cvt_pk_bf16_f32 v90, v12, v13
	v_cvt_pk_bf16_f32 v91, v14, v15
	s_nop 1
	v_permlane16_swap_b32_e32 v88, v90
	v_permlane16_swap_b32_e32 v89, v91
	s_nop 1
	global_store_dwordx4 v71, v[88:91], s[58:59] offset:0
	v_mul_f32_e32 v20, v20, v67
	v_mul_f32_e32 v21, v21, v67
	v_mul_f32_e32 v22, v22, v67
	v_mul_f32_e32 v23, v23, v67
	v_mul_f32_e32 v28, v28, v67
	v_mul_f32_e32 v29, v29, v67
	v_mul_f32_e32 v30, v30, v67
	v_mul_f32_e32 v31, v31, v67
	v_cvt_pk_bf16_f32 v92, v20, v21
	v_cvt_pk_bf16_f32 v93, v22, v23
	v_cvt_pk_bf16_f32 v94, v28, v29
	v_cvt_pk_bf16_f32 v95, v30, v31
	s_nop 1
	v_permlane16_swap_b32_e32 v92, v94
	v_permlane16_swap_b32_e32 v93, v95
	s_nop 1
	global_store_dwordx4 v71, v[92:95], s[58:59] offset:64
	v_mul_f32_e32 v36, v36, v67
	v_mul_f32_e32 v37, v37, v67
	v_mul_f32_e32 v38, v38, v67
	v_mul_f32_e32 v39, v39, v67
	v_mul_f32_e32 v44, v44, v67
	v_mul_f32_e32 v45, v45, v67
	v_mul_f32_e32 v46, v46, v67
	v_mul_f32_e32 v47, v47, v67
	v_cvt_pk_bf16_f32 v72, v36, v37
	v_cvt_pk_bf16_f32 v73, v38, v39
	v_cvt_pk_bf16_f32 v74, v44, v45
	v_cvt_pk_bf16_f32 v75, v46, v47
	s_nop 1
	v_permlane16_swap_b32_e32 v72, v74
	v_permlane16_swap_b32_e32 v73, v75
	s_nop 1
	global_store_dwordx4 v71, v[72:75], s[58:59] offset:128
	v_mul_f32_e32 v52, v52, v67
	v_mul_f32_e32 v53, v53, v67
	v_mul_f32_e32 v54, v54, v67
	v_mul_f32_e32 v55, v55, v67
	v_mul_f32_e32 v60, v60, v67
	v_mul_f32_e32 v61, v61, v67
	v_mul_f32_e32 v62, v62, v67
	v_mul_f32_e32 v63, v63, v67
	v_cvt_pk_bf16_f32 v76, v52, v53
	v_cvt_pk_bf16_f32 v77, v54, v55
	v_cvt_pk_bf16_f32 v78, v60, v61
	v_cvt_pk_bf16_f32 v79, v62, v63
	s_nop 1
	v_permlane16_swap_b32_e32 v76, v78
	v_permlane16_swap_b32_e32 v77, v79
	s_nop 1
	global_store_dwordx4 v71, v[76:79], s[58:59] offset:192
	s_barrier
